# C3 step: next step's log-decay column and state tile requested right after the state-tile LDS write (earlier than before)
# baseline (speedup 1.0000x reference)
; #define LAS __attribute__((address_space(3)))
; #define lds lds_hidden(lds0)
; __device__ __forceinline__ void c3_phase(LAS unsigned char* lds, const bf16_t* __restrict__ QH, const bf16_t* __restrict__ LF, const bf16_t* __restrict__ VTH, const bf16_t* __restrict__ SIN, ...
;     ...
;             float lfv[16], cs[16]; u32x4 stv[4];
; #pragma unroll
;             for (int i = 0; i < 16; ++i) lfv[i] = __uint_as_float(lfn[i] << 16);
; #pragma unroll
;             for (int i = 0; i < 4; ++i) stv[i] = stn[i];
;             float run = 0.f;
; #pragma unroll
;             for (int i = 0; i < 16; ++i) { run += lfv[i]; cs[i] = run; }
;             __syncthreads();
;             qtot[tq * 128 + d] = run;
; #pragma unroll
;             for (int i = 0; i < 4; ++i) { const int ch = tid + i * 512, e = ch >> 4, part = ch & 15;
;                 *(LAS u32x4*)(lds + C3_ST + e * R272 + part * 16) = stv[i]; }
;             __syncthreads();
.LBB0_1097:
	s_waitcnt vmcnt(19)
	v_lshlrev_b32_e32 v215, 16, v162
	v_mul_f32_e32 v215, 0x3fb8aa3b, v215
	s_waitcnt vmcnt(18)
	v_lshlrev_b32_e32 v220, 16, v164
	v_mul_f32_e32 v220, 0x3fb8aa3b, v220
	v_add_f32_e32 v224, 0, v215
	s_waitcnt vmcnt(17)
	v_lshlrev_b32_e32 v221, 16, v65
	v_mul_f32_e32 v221, 0x3fb8aa3b, v221
	v_add_f32_e32 v225, v224, v220
	s_waitcnt vmcnt(16)
	v_lshlrev_b32_e32 v222, 16, v166
	v_mul_f32_e32 v222, 0x3fb8aa3b, v222
	v_add_f32_e32 v226, v225, v221
	s_waitcnt vmcnt(15)
	v_lshlrev_b32_e32 v223, 16, v160
	v_mul_f32_e32 v223, 0x3fb8aa3b, v223
	v_add_f32_e32 v227, v226, v222
	s_waitcnt vmcnt(14)
	v_lshlrev_b32_e32 v213, 16, v161
	v_mul_f32_e32 v213, 0x3fb8aa3b, v213
	v_add_f32_e32 v228, v227, v223
	s_waitcnt vmcnt(13)
	v_lshlrev_b32_e32 v211, 16, v163
	v_mul_f32_e32 v211, 0x3fb8aa3b, v211
	v_add_f32_e32 v214, v228, v213
	s_waitcnt vmcnt(12)
	v_lshlrev_b32_e32 v209, 16, v169
	v_mul_f32_e32 v209, 0x3fb8aa3b, v209
	v_add_f32_e32 v212, v214, v211
	s_waitcnt vmcnt(11)
	v_lshlrev_b32_e32 v207, 16, v165
	v_mul_f32_e32 v207, 0x3fb8aa3b, v207
	v_add_f32_e32 v210, v212, v209
	s_waitcnt vmcnt(10)
	v_lshlrev_b32_e32 v51, 16, v167
	v_mul_f32_e32 v51, 0x3fb8aa3b, v51
	v_add_f32_e32 v208, v210, v207
	s_waitcnt vmcnt(9)
	v_lshlrev_b32_e32 v49, 16, v168
	v_mul_f32_e32 v49, 0x3fb8aa3b, v49
	v_add_f32_e32 v206, v208, v51
	s_waitcnt vmcnt(8)
	v_lshlrev_b32_e32 v47, 16, v172
	v_mul_f32_e32 v47, 0x3fb8aa3b, v47
	v_add_f32_e32 v50, v206, v49
	s_waitcnt vmcnt(7)
	v_lshlrev_b32_e32 v45, 16, v170
	v_mul_f32_e32 v45, 0x3fb8aa3b, v45
	v_add_f32_e32 v48, v50, v47
	s_waitcnt vmcnt(6)
	v_lshlrev_b32_e32 v43, 16, v171
	v_mul_f32_e32 v43, 0x3fb8aa3b, v43
	v_add_f32_e32 v46, v48, v45
	s_waitcnt vmcnt(5)
	v_lshlrev_b32_e32 v41, 16, v173
	v_mul_f32_e32 v41, 0x3fb8aa3b, v41
	v_add_f32_e32 v44, v46, v43
	s_waitcnt vmcnt(4)
	v_lshlrev_b32_e32 v37, 16, v174
	v_mul_f32_e32 v37, 0x3fb8aa3b, v37
	v_add_f32_e32 v42, v44, v41
	v_add_f32_e32 v38, v42, v37
	s_waitcnt lgkmcnt(0)
	s_barrier
	ds_write_b32 v175, v38
	s_waitcnt vmcnt(3)
	ds_write_b128 v181, v[2:5]
	s_waitcnt vmcnt(2)
	ds_write_b128 v182, v[6:9]
	s_waitcnt vmcnt(1)
	ds_write_b128 v183, v[10:13]
	s_waitcnt vmcnt(0)
	ds_write_b128 v184, v[14:17]
	s_waitcnt lgkmcnt(0)
	s_andn2_b64 vcc, exec, s[2:3]
	s_cbranch_vccz .Lc3pf_d0
	s_andn2_b64 vcc, exec, s[86:87]
	s_cbranch_vccnz .Lc3pf_done
	global_load_ushort v162, v[82:83], off
	global_load_ushort v164, v[82:83], off offset:2048
	global_load_ushort v65, v[84:85], off
	global_load_ushort v166, v[86:87], off
	global_load_ushort v160, v[88:89], off
	global_load_ushort v161, v[90:91], off
	global_load_ushort v163, v[92:93], off
	global_load_ushort v169, v[94:95], off
	global_load_ushort v165, v[96:97], off
	global_load_ushort v167, v[98:99], off
	global_load_ushort v168, v[100:101], off
	global_load_ushort v172, v[102:103], off
	global_load_ushort v170, v[104:105], off
	global_load_ushort v171, v[106:107], off
	global_load_ushort v173, v[108:109], off
	global_load_ushort v174, v[110:111], off
	global_load_dwordx4 v[2:5], v[112:113], off nt
	global_load_dwordx4 v[6:9], v[114:115], off nt
	global_load_dwordx4 v[10:13], v[116:117], off nt
	global_load_dwordx4 v[14:17], v[118:119], off nt
	s_branch .Lc3pf_done
.Lc3pf_d0:
	global_load_ushort v162, v[120:121], off offset:1024
	global_load_ushort v164, v[122:123], off offset:1024
	global_load_ushort v65, v[124:125], off offset:1024
	global_load_ushort v166, v[126:127], off offset:1024
	global_load_ushort v160, v[128:129], off offset:1024
	global_load_ushort v161, v[130:131], off offset:1024
	global_load_ushort v163, v[132:133], off offset:1024
	global_load_ushort v169, v[134:135], off offset:1024
	global_load_ushort v165, v[136:137], off offset:1024
	global_load_ushort v167, v[138:139], off offset:1024
	global_load_ushort v168, v[140:141], off offset:1024
	global_load_ushort v172, v[142:143], off offset:1024
	global_load_ushort v170, v[144:145], off offset:1024
	global_load_ushort v171, v[146:147], off offset:1024
	global_load_ushort v173, v[148:149], off offset:1024
	global_load_ushort v174, v[150:151], off offset:1024
	global_load_dwordx4 v[2:5], v[152:153], off nt
	global_load_dwordx4 v[6:9], v[154:155], off nt
	global_load_dwordx4 v[10:13], v[156:157], off nt
	global_load_dwordx4 v[14:17], v[158:159], off nt
; #define LAS __attribute__((address_space(3)))
; __device__ __forceinline__ bf16_t f2bf(float f) { unsigned u = __float_as_uint(f); u += 0x7FFFu + ((u >> 16) & 1u); return (bf16_t)(u >> 16); }
; __device__ __forceinline__ float fexp(float x) { return __builtin_amdgcn_exp2f(x * 1.4426950408889634f); }
; #define lds lds_hidden(lds0)
; __device__ __forceinline__ void c3_phase(LAS unsigned char* lds, const bf16_t* __restrict__ QH, const bf16_t* __restrict__ LF, const bf16_t* __restrict__ VTH, const bf16_t* __restrict__ SIN, ...
;     ...
;             const float q0 = qtot[d], q1 = qtot[128 + d], q2 = qtot[256 + d], q3 = qtot[384 + d];
;             const float pre = (tq > 0 ? q0 : 0.f) + (tq > 1 ? q1 : 0.f) + (tq > 2 ? q2 : 0.f), total = (q0 + q1) + (q2 + q3);
;             const float mref = dir == 0 ? (q0 + q1) : (q2 + q3);
; #pragma unroll
;             for (int i = 0; i < 16; ++i) {
;                 const int t = tq * 16 + i;
;                 const float bt = dir == 0 ? (pre + cs[i]) : (total - (pre + cs[i]) + lfv[i]);
;                 const float q = qv[i];
;                 const float key = 1.f - fexp(lfv[i]);
;                 *(LAS bf16_t*)(lds + C3_QT + t * R272 + d * 2) = f2bf(q * fexp(bt));
;                 *(LAS bf16_t*)(lds + C3_QH + t * R272 + d * 2) = f2bf(q * fexp(fminf(bt - mref, 80.f)));
;                 *(LAS bf16_t*)(lds + C3_KH + t * R272 + d * 2) = f2bf(key * fexp(fminf(mref - bt, 80.f)));
;             }
.Lc3pf_done:
	s_barrier
	ds_read2st64_b32 v[216:217], v176 offset1:2
	ds_read2st64_b32 v[218:219], v176 offset0:4 offset1:6
	s_xor_b64 s[78:79], s[2:3], -1
	s_and_b64 vcc, exec, s[78:79]
	s_mov_b64 s[92:93], -1
	s_waitcnt lgkmcnt(1)
	v_cndmask_b32_e64 v36, 0, v216, s[4:5]
	v_cndmask_b32_e64 v39, 0, v217, s[6:7]
	v_add_f32_e32 v36, v36, v39
	s_waitcnt lgkmcnt(0)
	v_cndmask_b32_e64 v39, 0, v218, s[8:9]
	v_add_f32_e32 v39, v36, v39
	v_add_f32_e32 v36, v216, v217
	v_add_f32_e32 v216, v218, v219
	v_add_f32_e32 v40, v36, v216
	v_cndmask_b32_e64 v231, -1.0, 1.0, s[2:3]
	v_cndmask_b32_e64 v232, v40, 0, s[2:3]
	v_cndmask_b32_e64 v233, 1.0, 0, s[2:3]
	v_cndmask_b32_e64 v36, v216, v36, s[2:3]
	v_add_f32_e32 v216, v224, v39
	v_fma_f32 v217, v231, v216, v232
	v_fma_f32 v216, v233, v215, v217
	v_exp_f32_e32 v217, v216
	v_exp_f32_e32 v215, v215
	v_add_f32_e32 v214, v214, v39
	v_mul_f32_e32 v234, v217, v190
	v_sub_f32_e32 v217, v216, v36
	v_max_f32_e32 v216, 0xc2e6d4ca, v217
	v_exp_f32_e64 v216, -v216
	v_min_f32_e32 v217, 0x42e6d4ca, v217
	v_exp_f32_e32 v217, v217
	v_fma_f32 v215, -v215, v216, v216
	v_cvt_pk_bf16_f32 v215, v215, v215
	ds_write_b16 v185, v215 offset:34816
	v_add_f32_e32 v215, v225, v39
	v_mul_f32_e32 v217, v217, v190
	v_fma_f32 v216, v231, v215, v232
	v_cvt_pk_bf16_f32 v217, v234, v217
	v_fma_f32 v215, v233, v220, v216
	ds_write_b16 v185, v217
	ds_write_b16_d16_hi v185, v217 offset:17408
	v_exp_f32_e32 v217, v215
	v_exp_f32_e32 v216, v220
	v_add_f32_e32 v212, v212, v39
	v_mul_f32_e32 v235, v217, v191
	v_sub_f32_e32 v217, v215, v36
	v_max_f32_e32 v215, 0xc2e6d4ca, v217
	v_exp_f32_e64 v215, -v215
	v_min_f32_e32 v217, 0x42e6d4ca, v217
	v_exp_f32_e32 v217, v217
	v_fma_f32 v215, -v216, v215, v215
	v_cvt_pk_bf16_f32 v215, v215, v215
	ds_write_b16 v185, v215 offset:35088
	v_add_f32_e32 v215, v226, v39
	v_mul_f32_e32 v217, v217, v191
	v_fma_f32 v216, v231, v215, v232
	v_cvt_pk_bf16_f32 v217, v235, v217
	v_fma_f32 v215, v233, v221, v216
	ds_write_b16 v185, v217 offset:272
	ds_write_b16_d16_hi v185, v217 offset:17680
	v_exp_f32_e32 v217, v215
	v_exp_f32_e32 v216, v221
	v_add_f32_e32 v210, v210, v39
	v_mul_f32_e32 v236, v217, v192
	v_sub_f32_e32 v217, v215, v36
	v_max_f32_e32 v215, 0xc2e6d4ca, v217
	v_exp_f32_e64 v215, -v215
	v_min_f32_e32 v217, 0x42e6d4ca, v217
	v_exp_f32_e32 v217, v217
	v_fma_f32 v215, -v216, v215, v215
	v_cvt_pk_bf16_f32 v215, v215, v215
	ds_write_b16 v185, v215 offset:35360
	v_add_f32_e32 v215, v227, v39
	v_mul_f32_e32 v217, v217, v192
	v_fma_f32 v216, v231, v215, v232
	v_cvt_pk_bf16_f32 v217, v236, v217
	v_fma_f32 v215, v233, v222, v216
	ds_write_b16 v185, v217 offset:544
	ds_write_b16_d16_hi v185, v217 offset:17952
	v_exp_f32_e32 v217, v215
	v_exp_f32_e32 v216, v222
	v_add_f32_e32 v208, v208, v39
	v_mul_f32_e32 v237, v217, v193
	v_sub_f32_e32 v217, v215, v36
	v_max_f32_e32 v215, 0xc2e6d4ca, v217
	v_exp_f32_e64 v215, -v215
	v_min_f32_e32 v217, 0x42e6d4ca, v217
	v_exp_f32_e32 v217, v217
	v_fma_f32 v215, -v216, v215, v215
	v_cvt_pk_bf16_f32 v215, v215, v215
	ds_write_b16 v185, v215 offset:35632
	v_add_f32_e32 v215, v228, v39
	v_mul_f32_e32 v217, v217, v193
	v_fma_f32 v216, v231, v215, v232
	v_cvt_pk_bf16_f32 v217, v237, v217
	v_fma_f32 v215, v233, v223, v216
	ds_write_b16 v185, v217 offset:816
	ds_write_b16_d16_hi v185, v217 offset:18224
	v_exp_f32_e32 v217, v215
	v_exp_f32_e32 v216, v223
	v_add_f32_e32 v206, v206, v39
	v_mul_f32_e32 v238, v217, v194
	v_sub_f32_e32 v217, v215, v36
	v_max_f32_e32 v215, 0xc2e6d4ca, v217
	v_exp_f32_e64 v215, -v215
	v_add_f32_e32 v50, v50, v39
	v_add_f32_e32 v48, v48, v39
	v_fma_f32 v215, -v216, v215, v215
	v_cvt_pk_bf16_f32 v215, v215, v215
	ds_write_b16 v185, v215 offset:35904
	v_fma_f32 v215, v231, v214, v232
	v_fma_f32 v214, v233, v213, v215
	v_exp_f32_e32 v215, v214
	v_exp_f32_e32 v213, v213
	v_add_f32_e32 v46, v46, v39
	v_mul_f32_e32 v239, v215, v195
	v_sub_f32_e32 v215, v214, v36
	v_max_f32_e32 v214, 0xc2e6d4ca, v215
	v_exp_f32_e64 v214, -v214
	v_add_f32_e32 v44, v44, v39
	v_add_f32_e32 v42, v42, v39
	v_fma_f32 v213, -v213, v214, v214
	v_cvt_pk_bf16_f32 v213, v213, v213
	ds_write_b16 v185, v213 offset:36176
	v_fma_f32 v213, v231, v212, v232
	v_fma_f32 v212, v233, v211, v213
	v_exp_f32_e32 v213, v212
	v_exp_f32_e32 v211, v211
	v_add_f32_e32 v38, v38, v39
	v_mul_f32_e32 v240, v213, v196
	v_sub_f32_e32 v213, v212, v36
	v_max_f32_e32 v212, 0xc2e6d4ca, v213
	v_exp_f32_e64 v212, -v212
	v_fma_f32 v39, v231, v38, v232
	v_fma_f32 v211, -v211, v212, v212
	v_cvt_pk_bf16_f32 v211, v211, v211
	ds_write_b16 v185, v211 offset:36448
	v_fma_f32 v211, v231, v210, v232
	v_fma_f32 v210, v233, v209, v211
	v_exp_f32_e32 v211, v210
	v_exp_f32_e32 v209, v209
	v_fma_f32 v38, v233, v37, v39
	v_mul_f32_e32 v241, v211, v197
	v_sub_f32_e32 v211, v210, v36
	v_max_f32_e32 v210, 0xc2e6d4ca, v211
	v_exp_f32_e64 v210, -v210
	v_exp_f32_e32 v39, v38
	v_fma_f32 v209, -v209, v210, v210
	v_cvt_pk_bf16_f32 v209, v209, v209
	ds_write_b16 v185, v209 offset:36720
	v_fma_f32 v209, v231, v208, v232
	v_fma_f32 v208, v233, v207, v209
	v_exp_f32_e32 v209, v208
	v_exp_f32_e32 v207, v207
	v_mul_f32_e32 v39, v39, v205
; #define LAS __attribute__((address_space(3)))
; __device__ __forceinline__ bf16_t f2bf(float f) { unsigned u = __float_as_uint(f); u += 0x7FFFu + ((u >> 16) & 1u); return (bf16_t)(u >> 16); }
; __device__ __forceinline__ float fexp(float x) { return __builtin_amdgcn_exp2f(x * 1.4426950408889634f); }
; #define lds lds_hidden(lds0)
; __device__ __forceinline__ void c3_phase(LAS unsigned char* lds, const bf16_t* __restrict__ QH, const bf16_t* __restrict__ LF, const bf16_t* __restrict__ VTH, const bf16_t* __restrict__ SIN, ...
;     ...
;             for (int i = 0; i < 16; ++i) {
;                 const int t = tq * 16 + i;
;                 const float bt = dir == 0 ? (pre + cs[i]) : (total - (pre + cs[i]) + lfv[i]);
;                 const float q = qv[i];
;                 const float key = 1.f - fexp(lfv[i]);
;                 *(LAS bf16_t*)(lds + C3_QT + t * R272 + d * 2) = f2bf(q * fexp(bt));
;                 *(LAS bf16_t*)(lds + C3_QH + t * R272 + d * 2) = f2bf(q * fexp(fminf(bt - mref, 80.f)));
;                 *(LAS bf16_t*)(lds + C3_KH + t * R272 + d * 2) = f2bf(key * fexp(fminf(mref - bt, 80.f)));
;             }
;             __syncthreads();
;             if (dir == 0) C3_PREFETCH(item, 1); else if (item + G < NB * 4 * 32) C3_PREFETCH(item + G, 0);
	v_mul_f32_e32 v242, v209, v198
	v_sub_f32_e32 v209, v208, v36
	v_max_f32_e32 v208, 0xc2e6d4ca, v209
	v_exp_f32_e64 v208, -v208
	v_min_f32_e32 v217, 0x42e6d4ca, v217
	v_min_f32_e32 v215, 0x42e6d4ca, v215
	v_fma_f32 v207, -v207, v208, v208
	v_cvt_pk_bf16_f32 v207, v207, v207
	ds_write_b16 v185, v207 offset:36992
	v_fma_f32 v207, v231, v206, v232
	v_fma_f32 v206, v233, v51, v207
	v_exp_f32_e32 v207, v206
	v_exp_f32_e32 v51, v51
	v_min_f32_e32 v213, 0x42e6d4ca, v213
	v_mul_f32_e32 v243, v207, v199
	v_sub_f32_e32 v207, v206, v36
	v_max_f32_e32 v206, 0xc2e6d4ca, v207
	v_exp_f32_e64 v206, -v206
	v_min_f32_e32 v211, 0x42e6d4ca, v211
	v_min_f32_e32 v209, 0x42e6d4ca, v209
	v_fma_f32 v51, -v51, v206, v206
	v_cvt_pk_bf16_f32 v51, v51, v51
	ds_write_b16 v185, v51 offset:37264
	v_fma_f32 v51, v231, v50, v232
	v_fma_f32 v50, v233, v49, v51
	v_exp_f32_e32 v51, v50
	v_exp_f32_e32 v49, v49
	v_min_f32_e32 v207, 0x42e6d4ca, v207
	v_mul_f32_e32 v244, v51, v200
	v_sub_f32_e32 v51, v50, v36
	v_max_f32_e32 v50, 0xc2e6d4ca, v51
	v_exp_f32_e64 v50, -v50
	v_min_f32_e32 v51, 0x42e6d4ca, v51
	v_fma_f32 v49, -v49, v50, v50
	v_cvt_pk_bf16_f32 v49, v49, v49
	ds_write_b16 v185, v49 offset:37536
	v_fma_f32 v49, v231, v48, v232
	v_fma_f32 v48, v233, v47, v49
	v_exp_f32_e32 v49, v48
	v_exp_f32_e32 v47, v47
	v_mul_f32_e32 v245, v49, v201
	v_sub_f32_e32 v49, v48, v36
	v_max_f32_e32 v48, 0xc2e6d4ca, v49
	v_exp_f32_e64 v48, -v48
	v_min_f32_e32 v49, 0x42e6d4ca, v49
	v_fma_f32 v47, -v47, v48, v48
	v_cvt_pk_bf16_f32 v47, v47, v47
	ds_write_b16 v185, v47 offset:37808
	v_fma_f32 v47, v231, v46, v232
	v_fma_f32 v46, v233, v45, v47
	v_exp_f32_e32 v47, v46
	v_exp_f32_e32 v45, v45
	v_mul_f32_e32 v246, v47, v202
	v_sub_f32_e32 v47, v46, v36
	v_max_f32_e32 v46, 0xc2e6d4ca, v47
	v_exp_f32_e64 v46, -v46
	v_min_f32_e32 v47, 0x42e6d4ca, v47
	v_fma_f32 v45, -v45, v46, v46
	v_cvt_pk_bf16_f32 v45, v45, v45
	ds_write_b16 v185, v45 offset:38080
	v_fma_f32 v45, v231, v44, v232
	v_fma_f32 v44, v233, v43, v45
	v_exp_f32_e32 v45, v44
	v_exp_f32_e32 v43, v43
	v_mul_f32_e32 v247, v45, v203
	v_sub_f32_e32 v45, v44, v36
	v_max_f32_e32 v44, 0xc2e6d4ca, v45
	v_exp_f32_e64 v44, -v44
	v_min_f32_e32 v45, 0x42e6d4ca, v45
	v_fma_f32 v43, -v43, v44, v44
	v_cvt_pk_bf16_f32 v43, v43, v43
	ds_write_b16 v185, v43 offset:38352
	v_fma_f32 v43, v231, v42, v232
	v_fma_f32 v42, v233, v41, v43
	v_exp_f32_e32 v43, v42
	v_cvt_pk_bf16_f32 v39, v39, v39
	ds_write_b16 v185, v39 offset:4080
	v_mul_f32_e32 v248, v43, v204
	v_sub_f32_e32 v43, v42, v36
	v_max_f32_e32 v42, 0xc2e6d4ca, v43
	v_sub_f32_e32 v39, v38, v36
	v_max_f32_e32 v36, 0xc2e6d4ca, v39
	v_min_f32_e32 v43, 0x42e6d4ca, v43
	v_min_f32_e32 v39, 0x42e6d4ca, v39
	v_exp_f32_e32 v41, v41
	v_exp_f32_e32 v37, v37
	v_exp_f32_e32 v217, v217
	v_exp_f32_e32 v215, v215
	v_exp_f32_e32 v213, v213
	v_exp_f32_e32 v211, v211
	v_exp_f32_e32 v209, v209
	v_exp_f32_e32 v207, v207
	v_exp_f32_e32 v51, v51
	v_exp_f32_e32 v49, v49
	v_exp_f32_e32 v47, v47
	v_exp_f32_e32 v45, v45
	v_exp_f32_e32 v43, v43
	v_exp_f32_e64 v42, -v42
	v_exp_f32_e32 v39, v39
	v_exp_f32_e64 v36, -v36
	v_mul_f32_e32 v217, v217, v194
	v_mul_f32_e32 v215, v215, v195
	v_mul_f32_e32 v213, v213, v196
	v_mul_f32_e32 v211, v211, v197
	v_mul_f32_e32 v209, v209, v198
	v_mul_f32_e32 v207, v207, v199
	v_mul_f32_e32 v51, v51, v200
	v_mul_f32_e32 v49, v49, v201
	v_mul_f32_e32 v47, v47, v202
	v_mul_f32_e32 v45, v45, v203
	v_mul_f32_e32 v43, v43, v204
	v_fma_f32 v41, -v41, v42, v42
	v_mul_f32_e32 v39, v39, v205
	v_fma_f32 v36, -v37, v36, v36
	v_cvt_pk_bf16_f32 v217, v238, v217
	v_cvt_pk_bf16_f32 v215, v239, v215
	v_cvt_pk_bf16_f32 v213, v240, v213
	v_cvt_pk_bf16_f32 v211, v241, v211
	v_cvt_pk_bf16_f32 v209, v242, v209
	v_cvt_pk_bf16_f32 v207, v243, v207
	v_cvt_pk_bf16_f32 v51, v244, v51
	v_cvt_pk_bf16_f32 v49, v245, v49
	v_cvt_pk_bf16_f32 v47, v246, v47
	v_cvt_pk_bf16_f32 v45, v247, v45
	v_cvt_pk_bf16_f32 v43, v248, v43
	v_cvt_pk_bf16_f32 v41, v41, v41
	v_cvt_pk_bf16_f32 v39, v39, v39
	v_cvt_pk_bf16_f32 v36, v36, v36
	ds_write_b16 v185, v217 offset:1088
	ds_write_b16_d16_hi v185, v217 offset:18496
	ds_write_b16 v185, v215 offset:1360
	ds_write_b16_d16_hi v185, v215 offset:18768
	ds_write_b16 v185, v213 offset:1632
	ds_write_b16_d16_hi v185, v213 offset:19040
	ds_write_b16 v185, v211 offset:1904
	ds_write_b16_d16_hi v185, v211 offset:19312
	ds_write_b16 v185, v209 offset:2176
	ds_write_b16_d16_hi v185, v209 offset:19584
	ds_write_b16 v185, v207 offset:2448
	ds_write_b16_d16_hi v185, v207 offset:19856
	ds_write_b16 v185, v51 offset:2720
	ds_write_b16_d16_hi v185, v51 offset:20128
	ds_write_b16 v185, v49 offset:2992
	ds_write_b16_d16_hi v185, v49 offset:20400
	ds_write_b16 v185, v47 offset:3264
	ds_write_b16_d16_hi v185, v47 offset:20672
	ds_write_b16 v185, v45 offset:3536
	ds_write_b16_d16_hi v185, v45 offset:20944
	ds_write_b16 v185, v43 offset:3808
	ds_write_b16_d16_hi v185, v43 offset:21216
	ds_write_b16 v185, v41 offset:38624
	ds_write_b16 v185, v39 offset:21488
	ds_write_b16 v185, v36 offset:38896
	s_waitcnt lgkmcnt(0)
	s_barrier
	s_cbranch_vccz .LBB0_1101
	s_andn2_b64 vcc, exec, s[86:87]
	s_cbranch_vccnz .LBB0_1100

; __device__ __forceinline__ void c3_phase(LAS unsigned char* lds, const bf16_t* __restrict__ QH, const bf16_t* __restrict__ LF, const bf16_t* __restrict__ VTH, const bf16_t* __restrict__ SIN, ...
;     ...
;             if (dir == 0) C3_PREFETCH(item, 1); else if (item + G < NB * 4 * 32) C3_PREFETCH(item + G, 0);
.LBB0_1101:
	s_andn2_b64 vcc, exec, s[92:93]
	s_mov_b64 s[92:93], s[12:13]
	s_cbranch_vccnz .LBB0_1103
	s_mov_b64 s[92:93], -1
